# sliding-window units assigned statically as well (units id and id + 256): no device-atomic claims left in the attention unit queues; the gate tiles remain the dynamic filler
# baseline (speedup 1.0000x reference)
; __device__ __forceinline__ int lane_id() { unsigned m = ~0u; asm volatile("" : "+s"(m)); return (int)__builtin_amdgcn_mbcnt_hi(m, __builtin_amdgcn_mbcnt_lo(m, 0u)); }
; __device__ __forceinline__ void claim_fire(unsigned* ctr, int tid, int* pend) { if (tid == 0) *pend = (int)__hip_atomic_fetch_add(ctr, 1u, __ATOMIC_RELAXED, __HIP_MEMORY_SCOPE_AGENT); }
;     ...
;     unsigned* q2ctr = F.ctl + CW_QUEUE + ((l + qlo) * 8 + 2 + qs) * 64; unsigned* q3ctr = F.ctl + CW_QUEUE + ((l + qlo) * 8 + 3 + qs) * 64;
;     const float* slopes8 = (const float*)(F.ctl + CW_LAM) + 16; const float* sinks = a->in[7] + l * 8;
;     at::claim_fire(q3ctr, F.tid, &pend);
;     if (qmask & 4) for (;;) {
;         const int idx = at::claim_take(lds, F.tid, &pend); if (idx >= 256) break;
;         const int qb = 31 - (idx >> 3), bh = idx & 7, b = bh >> 2, h = bh & 3;
;         const bf16_t* Hb = H + (size_t)b * S * HP;
;         at::Tens T{Hb + C_SB + h * 64, Hb + C_SB + 256 + h * 64, Hb + C_SB + 512 + h * 64, HP, HP, HP};
;         at::sb_unit(lds, wv, lane_id(), T, qb * 256, O + (size_t)b * S * OP + 256 + h * 64, OP, q3ctr, &pend);
;     }
;     at::claim_fire(q2ctr, F.tid, &pend);
.LBB0_1019:
	s_add_u32 s14, s52, 0x200
	s_addc_u32 s15, s53, 0
	v_writelane_b32 v255, s14, 3
	s_nop 1
	v_writelane_b32 v255, s15, 4
	s_and_saveexec_b64 s[14:15], s[38:39]
	s_cbranch_execz .LBB0_1023
	s_mov_b64 s[34:35], exec
	v_mbcnt_lo_u32_b32 v0, s34, 0
	v_mbcnt_hi_u32_b32 v0, s35, v0
	v_cmp_eq_u32_e32 vcc, 0, v0
	s_and_saveexec_b64 s[16:17], vcc
	s_cbranch_execz .LBB0_1022
	s_nop 0
	v_readlane_b32 s20, v255, 3
	v_mov_b32_e32 v1, s92
	v_readlane_b32 s21, v255, 4
	v_mov_b32_e32 v192, s92
	s_nop 0
	s_nop 0

;     ...
;     if (nctr != nullptr && tid == 0) *pend = (int)__hip_atomic_fetch_add(nctr, 1u, __ATOMIC_RELAXED, __HIP_MEMORY_SCOPE_AGENT);
.LBB0_1065:
	v_cmp_eq_u32_e32 vcc, 0, v118
	s_and_b64 s[28:29], s[14:15], vcc
	s_and_saveexec_b64 s[40:41], s[28:29]
	v_readlane_b32 s92, v254, 59
	v_readlane_b32 s93, v254, 60
	v_readlane_b32 s95, v254, 61
	s_cbranch_execz .LBB0_1025
	s_mov_b64 s[44:45], exec
	v_mbcnt_lo_u32_b32 v0, s44, 0
	v_mbcnt_hi_u32_b32 v0, s45, v0
	v_cmp_eq_u32_e32 vcc, 0, v0
	s_and_saveexec_b64 s[42:43], vcc
	s_cbranch_execz .LBB0_1024
	v_add_u32_e32 v192, 0x100, v192
	v_mov_b32_e32 v1, v192
	v_readlane_b32 s28, v255, 3
	v_readlane_b32 s29, v255, 4
	s_nop 0
	s_nop 0
	s_branch .LBB0_1024
